# final combine/LN2 row loop: the f32 output row passes through a per-wave LDS image so each global_store_dwordx4 writes 1 KiB contiguous (was 64 pieces at 64-byte stride)
# speedup vs baseline: 1.0366x; 1.0097x over previous
; #define LAS __attribute__((address_space(3)))
; #define REPS(k) for (int _rep = 0; _rep < ((MK_DUP == (k) || (MK_DUP == 202 && (k) == 0)) ? 2 : 1); ++_rep)
; __global__ void __launch_bounds__(NW * 64, 2) mk_fwd(Args args) {
;     ...
;     REPS(12) if (IN(12)) { PH_BEGIN
;         LAS float* cv = (LAS float*)lds; int curb = -1;
;         for (int c = bx; c < M / 256; c += G) {
;             const int b = c >> 3;
;             if (b != curb) {
;                 __syncthreads();
;                 if (tid < 256) { const int i = tid * 4; *(LAS f32x4*)(cv + i) = *(const f32x4*)(X.ln1_g + i); *(LAS f32x4*)(cv + 1024 + i) = *(const f32x4*)(X.ln1_b + i);
;                     *(LAS f32x4*)(cv + 2048 + i) = *(const f32x4*)(X.ln2_g + i); *(LAS f32x4*)(cv + 3072 + i) = *(const f32x4*)(X.ln2_b + i); *(LAS f32x4*)(cv + 4096 + i) = *(const f32x4*)(mod + b * 6144 + MOD_GATE_F + i); }
;                 __syncthreads(); curb = b;
;             }
;             const int r0 = c * 256 + wave * 32;
;             RowRaw nx; final_load(nx, (const bf16_t*)(ws + WS_TB), ybuf, ws + WS_YSH, (const float*)(ws + WS_STATS), r0, lane);
; #pragma unroll 1
;             for (int i = 0; i < 32; ++i) {
;                 const RowRaw cur = nx;
;                 final_load(nx, (const bf16_t*)(ws + WS_TB), ybuf, ws + WS_YSH, (const float*)(ws + WS_STATS), r0 + (i < 31 ? i + 1 : i), lane);
;                 final_row(out, cur, cv, r0 + i, lane);
.LBB0_848:
	s_cmp_lt_i32 s92, 13
	s_cselect_b64 s[0:1], -1, 0
	s_and_b64 s[0:1], s[0:1], s[8:9]
	s_andn2_b64 vcc, exec, s[0:1]
	s_cbranch_vccnz .LBB0_858
	s_mov_b64 s[2:3], s[90:91]
	s_and_b64 vcc, exec, s[96:97]
	s_cbranch_vccnz .LBB0_858
	s_load_dwordx4 s[4:7], s[2:3], 0xa8
	s_load_dword s9, s[90:91], 0xc0
	v_mbcnt_lo_u32_b32 v0, -1, 0
	v_mbcnt_hi_u32_b32 v4, -1, v0
	s_and_b32 s0, s88, 0xffffffc0
	v_mov_b32_e32 v45, 0
	v_add_u32_e32 v2, s0, v4
	s_movk_i32 s0, 0x100
	v_lshlrev_b32_e32 v44, 4, v4
	v_cmp_gt_i32_e64 s[0:1], s0, v2
	v_lshlrev_b32_e32 v0, 2, v2
	v_lshl_add_u32 v204, v2, 4, 0
	s_waitcnt lgkmcnt(0)
	v_lshl_add_u64 v[2:3], s[6:7], 0, v[44:45]
	s_mov_b64 s[12:13], 0xa000000
	v_lshl_add_u64 v[46:47], v[2:3], 0, s[12:13]
	s_mov_b64 s[12:13], 0x3a000000
	v_lshl_add_u64 v[48:49], v[2:3], 0, s[12:13]
	v_lshlrev_b32_e32 v2, 5, v4
	v_mov_b32_e32 v3, v45
	s_lshl_b32 s11, s89, 5
	v_lshl_add_u64 v[2:3], s[6:7], 0, v[2:3]
	s_mov_b64 s[12:13], 0x32000000
	s_add_u32 s16, s6, 0x1800000
	v_lshl_add_u64 v[50:51], v[2:3], 0, s[12:13]
	v_lshlrev_b32_e32 v2, 6, v4
	v_mov_b32_e32 v3, v45
	v_ashrrev_i32_e32 v1, 31, v0
	s_addc_u32 s17, s7, 0
	v_lshl_add_u64 v[52:53], s[4:5], 0, v[2:3]
	v_lshlrev_b32_e32 v210, 4, v4
	v_mov_b32_e32 v211, 0
	v_lshl_add_u64 v[210:211], s[4:5], 0, v[210:211]
	s_mul_i32 s12, s89, 0x1400
	s_add_i32 s12, s12, 0x8000
	v_mul_u32_u24_e32 v208, 0x50, v4
	v_add_u32_e32 v208, s12, v208
	v_lshrrev_b32_e32 v209, 2, v4
	v_mul_u32_u24_e32 v209, 0x50, v209
	v_and_b32_e32 v212, 3, v4
	v_lshl_add_u32 v209, v212, 4, v209
	v_add_u32_e32 v209, s12, v209
	s_lshl_b32 s4, s44, 8
	s_mov_b32 s22, -1
	s_add_i32 s18, s4, s11
	s_lshl_b32 s19, s9, 8
	v_lshlrev_b64 v[54:55], 2, v[0:1]
	s_movk_i32 s20, 0x1000
	s_mov_b32 s8, 0x3c800000
	s_mov_b32 s10, 0x3f9837f0
	v_mov_b32_e32 v205, 0x3727c5ac
	s_mov_b32 s21, 0xf800000
	v_mov_b32_e32 v206, 0x260

; #define LAS __attribute__((address_space(3)))
; __device__ __forceinline__ void final_row(float* __restrict__ out, const RowRaw& R, const LAS float* cv  , int row, int lane) {
;     asm volatile("" : "+v"(cv));
;     const int c0 = lane * 16;
;     f32x4 a[4], t[4], v[4]; float s = 0.f;
; #pragma unroll
;     for (int j = 0; j < 4; ++j) a[j] = (f32x4){0.f, 0.f, 0.f, 0.f};
; #pragma unroll
;     for (int k = 0; k < 9; ++k) { const unsigned w[4] = {R.y[k].x, R.y[k].y, R.y[k].z, R.y[k].w};
; #pragma unroll
;         for (int j = 0; j < 4; ++j) { const f32x2 lo = __builtin_amdgcn_cvt_pk_f32_fp8((int)w[j], false), hi = __builtin_amdgcn_cvt_pk_f32_fp8((int)w[j], true); a[j].x += lo.x; a[j].y += lo.y; a[j].z += hi.x; a[j].w += hi.y; } }
;     unpack_t16r(R.t[0], R.t[1], t);
; #pragma unroll
;     for (int j = 0; j < 4; ++j) { const int col = c0 + 4 * j;
;         const f32x4 x1 = (t[j] - R.st.x) * R.st.y * *(const LAS f32x4*)(cv + col) + *(const LAS f32x4*)(cv + 1024 + col);
.LBB0_856:
	s_add_i32 s13, s23, 1
	s_cmp_lg_u32 s23, 31
	s_waitcnt vmcnt(0)
	v_cvt_pk_f32_fp8_e32 v[192:193], v40
	v_cvt_pk_f32_fp8_sdwa v[194:195], v40 src0_sel:WORD_1
	v_cvt_pk_f32_fp8_e32 v[196:197], v41
	v_cvt_pk_f32_fp8_sdwa v[198:199], v41 src0_sel:WORD_1
	v_cvt_pk_f32_fp8_e32 v[200:201], v42
	v_cvt_pk_f32_fp8_sdwa v[202:203], v42 src0_sel:WORD_1
	v_cvt_pk_f32_fp8_e32 v[180:181], v43
	v_cvt_pk_f32_fp8_sdwa v[182:183], v43 src0_sel:WORD_1
	s_cselect_b32 s4, s13, 31
	v_cvt_pk_f32_fp8_e32 v[156:157], v36
	v_cvt_pk_f32_fp8_sdwa v[164:165], v36 src0_sel:WORD_1
	v_cvt_pk_f32_fp8_e32 v[158:159], v37
	v_cvt_pk_f32_fp8_sdwa v[172:173], v37 src0_sel:WORD_1
	v_cvt_pk_f32_fp8_e32 v[166:167], v38
	v_cvt_pk_f32_fp8_sdwa v[184:185], v38 src0_sel:WORD_1
	v_cvt_pk_f32_fp8_e32 v[174:175], v39
	v_cvt_pk_f32_fp8_sdwa v[190:191], v39 src0_sel:WORD_1
	s_add_i32 s4, s4, s12
	v_cvt_pk_f32_fp8_e32 v[160:161], v32
	v_cvt_pk_f32_fp8_sdwa v[162:163], v32 src0_sel:WORD_1
	v_cvt_pk_f32_fp8_e32 v[168:169], v33
	v_cvt_pk_f32_fp8_sdwa v[170:171], v33 src0_sel:WORD_1
	v_cvt_pk_f32_fp8_e32 v[176:177], v34
	v_cvt_pk_f32_fp8_sdwa v[178:179], v34 src0_sel:WORD_1
	v_cvt_pk_f32_fp8_e32 v[186:187], v35
	v_cvt_pk_f32_fp8_sdwa v[188:189], v35 src0_sel:WORD_1
	v_cvt_pk_f32_fp8_e32 v[140:141], v12
	v_cvt_pk_f32_fp8_sdwa v[144:145], v12 src0_sel:WORD_1
	v_cvt_pk_f32_fp8_e32 v[142:143], v13
	v_cvt_pk_f32_fp8_sdwa v[148:149], v13 src0_sel:WORD_1
	v_cvt_pk_f32_fp8_e32 v[146:147], v14
	v_cvt_pk_f32_fp8_sdwa v[152:153], v14 src0_sel:WORD_1
	v_cvt_pk_f32_fp8_e32 v[150:151], v15
	v_cvt_pk_f32_fp8_sdwa v[154:155], v15 src0_sel:WORD_1
	v_cvt_pk_f32_fp8_e32 v[96:97], v8
	v_cvt_pk_f32_fp8_sdwa v[112:113], v8 src0_sel:WORD_1
	v_cvt_pk_f32_fp8_e32 v[106:107], v9
	v_cvt_pk_f32_fp8_sdwa v[116:117], v9 src0_sel:WORD_1
	v_cvt_pk_f32_fp8_e32 v[114:115], v10
	v_cvt_pk_f32_fp8_sdwa v[120:121], v10 src0_sel:WORD_1
	v_cvt_pk_f32_fp8_e32 v[118:119], v11
	v_cvt_pk_f32_fp8_sdwa v[122:123], v11 src0_sel:WORD_1
	v_cvt_pk_f32_fp8_e32 v[98:99], v4
	v_cvt_pk_f32_fp8_sdwa v[100:101], v4 src0_sel:WORD_1
	v_cvt_pk_f32_fp8_e32 v[80:81], v5
	v_cvt_pk_f32_fp8_sdwa v[82:83], v5 src0_sel:WORD_1
	v_cvt_pk_f32_fp8_e32 v[84:85], v6
	v_cvt_pk_f32_fp8_sdwa v[86:87], v6 src0_sel:WORD_1
	v_cvt_pk_f32_fp8_e32 v[76:77], v7
	v_cvt_pk_f32_fp8_sdwa v[78:79], v7 src0_sel:WORD_1
	v_cvt_pk_f32_fp8_e32 v[32:33], v0
	v_cvt_pk_f32_fp8_sdwa v[36:37], v0 src0_sel:WORD_1
	v_cvt_pk_f32_fp8_e32 v[34:35], v1
	v_cvt_pk_f32_fp8_sdwa v[40:41], v1 src0_sel:WORD_1
	v_cvt_pk_f32_fp8_e32 v[38:39], v2
	v_cvt_pk_f32_fp8_sdwa v[56:57], v2 src0_sel:WORD_1
	v_cvt_pk_f32_fp8_e32 v[42:43], v3
	v_cvt_pk_f32_fp8_sdwa v[58:59], v3 src0_sel:WORD_1
	v_lshlrev_b32_e32 v2, 16, v24
	v_and_b32_e32 v3, 0xffff0000, v24
	v_lshlrev_b32_e32 v0, 16, v25
	v_and_b32_e32 v1, 0xffff0000, v25
	v_lshlrev_b32_e32 v6, 16, v26
	v_and_b32_e32 v7, 0xffff0000, v26
	v_lshlrev_b32_e32 v4, 16, v27
	v_and_b32_e32 v5, 0xffff0000, v27
	v_lshlrev_b32_e32 v8, 16, v20
	v_and_b32_e32 v9, 0xffff0000, v20
	v_lshlrev_b32_e32 v10, 16, v21
	v_and_b32_e32 v11, 0xffff0000, v21
	v_lshlrev_b32_e32 v12, 16, v22
	v_and_b32_e32 v13, 0xffff0000, v22
	v_lshlrev_b32_e32 v14, 16, v23
	v_and_b32_e32 v15, 0xffff0000, v23
	s_ashr_i32 s5, s4, 31
	v_sub_f32_e32 v1, v1, v136
	v_sub_f32_e32 v0, v0, v136
	v_sub_f32_e32 v3, v3, v136
	v_sub_f32_e32 v2, v2, v136
	v_sub_f32_e32 v5, v5, v136
	v_sub_f32_e32 v4, v4, v136
	v_sub_f32_e32 v7, v7, v136
	v_sub_f32_e32 v6, v6, v136
	v_sub_f32_e32 v9, v9, v136
	v_sub_f32_e32 v8, v8, v136
	v_sub_f32_e32 v11, v11, v136
	v_sub_f32_e32 v10, v10, v136
	v_sub_f32_e32 v13, v13, v136
	v_sub_f32_e32 v12, v12, v136
	v_sub_f32_e32 v15, v15, v136
	v_sub_f32_e32 v14, v14, v136
	s_lshl_b64 s[14:15], s[4:5], 13
	v_cvt_pk_f32_fp8_e32 v[60:61], v16
	v_cvt_pk_f32_fp8_sdwa v[62:63], v16 src0_sel:WORD_1
	v_cvt_pk_f32_fp8_e32 v[64:65], v17
	v_cvt_pk_f32_fp8_sdwa v[66:67], v17 src0_sel:WORD_1
	v_pk_mul_f32 v[132:133], v[136:137], v[2:3] op_sel:[1,0]
	v_pk_mul_f32 v[138:139], v[136:137], v[0:1] op_sel:[1,0]
	v_pk_mul_f32 v[128:129], v[136:137], v[6:7] op_sel:[1,0]
	v_pk_mul_f32 v[134:135], v[136:137], v[4:5] op_sel:[1,0]
	v_pk_mul_f32 v[124:125], v[136:137], v[10:11] op_sel:[1,0]
	v_pk_mul_f32 v[130:131], v[136:137], v[8:9] op_sel:[1,0]
	v_pk_mul_f32 v[126:127], v[136:137], v[14:15] op_sel:[1,0]
	v_pk_mul_f32 v[136:137], v[136:137], v[12:13] op_sel:[1,0]
	v_pk_add_f32 v[0:1], v[192:193], 0 op_sel_hi:[1,0]
	v_pk_add_f32 v[2:3], v[194:195], 0 op_sel_hi:[1,0]
	v_pk_add_f32 v[4:5], v[196:197], 0 op_sel_hi:[1,0]
	v_pk_add_f32 v[6:7], v[198:199], 0 op_sel_hi:[1,0]
	v_pk_add_f32 v[8:9], v[200:201], 0 op_sel_hi:[1,0]
	v_pk_add_f32 v[10:11], v[202:203], 0 op_sel_hi:[1,0]
	v_pk_add_f32 v[12:13], v[180:181], 0 op_sel_hi:[1,0]
	v_pk_add_f32 v[14:15], v[182:183], 0 op_sel_hi:[1,0]
	v_lshl_add_u64 v[16:17], v[46:47], 0, s[14:15]
	s_lshl_b64 s[24:25], s[4:5], 10
	s_lshl_b64 s[26:27], s[4:5], 11
	s_lshl_b64 s[4:5], s[4:5], 3
	v_pk_add_f32 v[2:3], v[2:3], v[164:165]
	v_pk_add_f32 v[0:1], v[0:1], v[156:157]
	v_pk_add_f32 v[6:7], v[6:7], v[172:173]
	v_pk_add_f32 v[4:5], v[4:5], v[158:159]
	v_pk_add_f32 v[10:11], v[10:11], v[184:185]
	v_pk_add_f32 v[8:9], v[8:9], v[166:167]
	v_pk_add_f32 v[14:15], v[14:15], v[190:191]
	v_pk_add_f32 v[12:13], v[12:13], v[174:175]
	v_add_co_u32_e32 v156, vcc, s20, v16
	v_cvt_pk_f32_fp8_e32 v[88:89], v28
	v_cvt_pk_f32_fp8_sdwa v[90:91], v28 src0_sel:WORD_1
	v_cvt_pk_f32_fp8_e32 v[92:93], v29
	v_cvt_pk_f32_fp8_sdwa v[94:95], v29 src0_sel:WORD_1
	v_cvt_pk_f32_fp8_e32 v[102:103], v30
	v_cvt_pk_f32_fp8_sdwa v[104:105], v30 src0_sel:WORD_1
	v_cvt_pk_f32_fp8_e32 v[108:109], v31
; #define LAS __attribute__((address_space(3)))
; __device__ __forceinline__ void final_load(RowRaw& R, const bf16_t* __restrict__ tb, const unsigned char* __restrict__ ybuf, const unsigned char* __restrict__ ysh, const float* __restrict__ stats, int row, int lane) {
;     const int c0 = lane * 16;
; #pragma unroll
;     for (int k = 0; k < TOPK; ++k) R.y[k] = __builtin_nontemporal_load((const u32x4*)(ybuf + ((size_t)row * TOPK + k) * D + c0));
;     R.y[8] = __builtin_nontemporal_load((const u32x4*)(ysh + (size_t)row * D + c0));
;     R.t[0] = __builtin_nontemporal_load((const u32x4*)(tb + (size_t)row * D + c0)); R.t[1] = __builtin_nontemporal_load((const u32x4*)(tb + (size_t)row * D + c0 + 8));
;     R.st = *(const f32x2*)(stats + 2 * (size_t)row);
; }
; __device__ __forceinline__ void final_row(float* __restrict__ out, const RowRaw& R, const LAS float* cv  , int row, int lane) {
;     asm volatile("" : "+v"(cv));
;     const int c0 = lane * 16;
;     f32x4 a[4], t[4], v[4]; float s = 0.f;
; #pragma unroll
;     for (int j = 0; j < 4; ++j) a[j] = (f32x4){0.f, 0.f, 0.f, 0.f};
; #pragma unroll
;     for (int k = 0; k < 9; ++k) { const unsigned w[4] = {R.y[k].x, R.y[k].y, R.y[k].z, R.y[k].w};
; #pragma unroll
;         for (int j = 0; j < 4; ++j) { const f32x2 lo = __builtin_amdgcn_cvt_pk_f32_fp8((int)w[j], false), hi = __builtin_amdgcn_cvt_pk_f32_fp8((int)w[j], true); a[j].x += lo.x; a[j].y += lo.y; a[j].z += hi.x; a[j].w += hi.y; } }
;     unpack_t16r(R.t[0], R.t[1], t);
; #pragma unroll
;     for (int j = 0; j < 4; ++j) { const int col = c0 + 4 * j;
;         const f32x4 x1 = (t[j] - R.st.x) * R.st.y * *(const LAS f32x4*)(cv + col) + *(const LAS f32x4*)(cv + 1024 + col);
;         v[j] = x1 * ALPHA + *(const LAS f32x4*)(cv + 4096 + col) * a[j] * YINV;
;         s += (v[j].x + v[j].y) + (v[j].z + v[j].w); }
	v_cvt_pk_f32_fp8_sdwa v[110:111], v31 src0_sel:WORD_1
	v_cvt_pk_f32_fp8_e32 v[68:69], v18
	v_cvt_pk_f32_fp8_sdwa v[70:71], v18 src0_sel:WORD_1
	v_cvt_pk_f32_fp8_e32 v[72:73], v19
	v_cvt_pk_f32_fp8_sdwa v[74:75], v19 src0_sel:WORD_1
	v_lshl_add_u64 v[18:19], v[48:49], 0, s[24:25]
	v_lshl_add_u64 v[24:25], v[50:51], 0, s[26:27]
	s_add_u32 s14, s16, s4
	v_pk_add_f32 v[28:29], v[0:1], v[160:161]
	v_pk_add_f32 v[30:31], v[2:3], v[162:163]
	v_pk_add_f32 v[158:159], v[4:5], v[168:169]
	v_pk_add_f32 v[160:161], v[6:7], v[170:171]
	v_pk_add_f32 v[162:163], v[8:9], v[176:177]
	v_pk_add_f32 v[164:165], v[10:11], v[178:179]
	v_pk_add_f32 v[166:167], v[12:13], v[186:187]
	v_pk_add_f32 v[168:169], v[14:15], v[188:189]
	global_load_dwordx4 v[0:3], v[16:17], off nt
	global_load_dwordx4 v[4:7], v[16:17], off offset:1024 nt
	global_load_dwordx4 v[8:11], v[16:17], off offset:2048 nt
	global_load_dwordx4 v[12:15], v[16:17], off offset:3072 nt
	v_addc_co_u32_e32 v157, vcc, 0, v17, vcc
	global_load_dwordx4 v[20:23], v[24:25], off offset:16 nt
	s_nop 0
	global_load_dwordx4 v[16:19], v[18:19], off nt
	s_nop 0
	global_load_dwordx4 v[24:27], v[24:25], off nt
	s_addc_u32 s15, s17, s5
	v_pk_add_f32 v[170:171], v[30:31], v[144:145]
	v_pk_add_f32 v[172:173], v[28:29], v[140:141]
	v_pk_add_f32 v[160:161], v[160:161], v[148:149]
	v_pk_add_f32 v[158:159], v[158:159], v[142:143]
	v_pk_add_f32 v[152:153], v[164:165], v[152:153]
	v_pk_add_f32 v[162:163], v[162:163], v[146:147]
	v_pk_add_f32 v[164:165], v[166:167], v[150:151]
	global_load_dwordx4 v[28:31], v[156:157], off nt
	global_load_dwordx4 v[140:143], v[156:157], off offset:1024 nt
	global_load_dwordx4 v[144:147], v[156:157], off offset:2048 nt
	global_load_dwordx4 v[148:151], v[156:157], off offset:3072 nt
	global_load_dwordx2 v[188:189], v45, s[14:15]
	v_mov_b32_e32 v207, 0
	v_pk_add_f32 v[154:155], v[168:169], v[154:155]
	v_pk_add_f32 v[88:89], v[172:173], v[88:89]
	v_pk_add_f32 v[90:91], v[170:171], v[90:91]
	v_pk_add_f32 v[92:93], v[158:159], v[92:93]
	v_pk_add_f32 v[94:95], v[160:161], v[94:95]
	v_pk_add_f32 v[102:103], v[162:163], v[102:103]
	v_pk_add_f32 v[104:105], v[152:153], v[104:105]
	v_pk_add_f32 v[108:109], v[164:165], v[108:109]
	v_pk_add_f32 v[110:111], v[154:155], v[110:111]
	v_lshl_add_u32 v184, v44, 2, v207
	v_pk_add_f32 v[112:113], v[90:91], v[112:113]
	v_pk_add_f32 v[96:97], v[88:89], v[96:97]
	v_pk_add_f32 v[152:153], v[94:95], v[116:117]
	v_pk_add_f32 v[154:155], v[92:93], v[106:107]
	v_pk_add_f32 v[156:157], v[104:105], v[120:121]
	v_pk_add_f32 v[158:159], v[102:103], v[114:115]
	v_pk_add_f32 v[122:123], v[110:111], v[122:123]
	v_pk_add_f32 v[160:161], v[108:109], v[118:119]
	ds_read_b128 v[88:91], v184
	ds_read_b128 v[92:95], v184 offset:16
	ds_read_b128 v[102:105], v184 offset:32
	ds_read_b128 v[106:109], v184 offset:48
	v_pk_add_f32 v[190:191], v[96:97], v[98:99]
	v_pk_add_f32 v[100:101], v[112:113], v[100:101]
	ds_read_b128 v[96:99], v184 offset:4096
	ds_read_b128 v[110:113], v184 offset:4112
	ds_read_b128 v[114:117], v184 offset:16384
	ds_read_b128 v[118:121], v184 offset:16400
	v_pk_add_f32 v[192:193], v[154:155], v[80:81]
	v_pk_add_f32 v[194:195], v[152:153], v[82:83]
	v_pk_add_f32 v[196:197], v[158:159], v[84:85]
	v_pk_add_f32 v[198:199], v[156:157], v[86:87]
	ds_read_b128 v[80:83], v184 offset:4128
	ds_read_b128 v[84:87], v184 offset:4144
	ds_read_b128 v[152:155], v184 offset:16416
	ds_read_b128 v[156:159], v184 offset:16432
	v_pk_add_f32 v[36:37], v[100:101], v[36:37]
	v_pk_add_f32 v[32:33], v[190:191], v[32:33]
	v_pk_add_f32 v[40:41], v[194:195], v[40:41]
	v_pk_add_f32 v[34:35], v[192:193], v[34:35]
	v_pk_add_f32 v[32:33], v[32:33], v[60:61]
	v_pk_add_f32 v[36:37], v[36:37], v[62:63]
	v_pk_add_f32 v[34:35], v[34:35], v[64:65]
	v_pk_add_f32 v[40:41], v[40:41], v[66:67]
	v_pk_add_f32 v[200:201], v[160:161], v[76:77]
	v_pk_add_f32 v[122:123], v[122:123], v[78:79]
	s_waitcnt lgkmcnt(5)
	v_pk_mul_f32 v[36:37], v[36:37], v[116:117]
	v_pk_mul_f32 v[32:33], v[32:33], v[114:115]
	s_waitcnt lgkmcnt(4)
	v_pk_mul_f32 v[40:41], v[40:41], v[120:121]
	v_pk_mul_f32 v[34:35], v[34:35], v[118:119]
	v_pk_add_f32 v[56:57], v[198:199], v[56:57]
	v_pk_add_f32 v[38:39], v[196:197], v[38:39]
	v_pk_add_f32 v[58:59], v[122:123], v[58:59]
	v_pk_add_f32 v[42:43], v[200:201], v[42:43]
	v_pk_fma_f32 v[60:61], v[138:139], v[90:91], v[98:99]
	v_pk_fma_f32 v[62:63], v[132:133], v[88:89], v[96:97]
	v_pk_fma_f32 v[64:65], v[134:135], v[94:95], v[112:113]
	v_pk_fma_f32 v[66:67], v[128:129], v[92:93], v[110:111]
	v_pk_mul_f32 v[36:37], v[36:37], s[8:9] op_sel_hi:[1,0]
	v_pk_mul_f32 v[32:33], v[32:33], s[8:9] op_sel_hi:[1,0]
	v_pk_mul_f32 v[40:41], v[40:41], s[8:9] op_sel_hi:[1,0]
	v_pk_mul_f32 v[34:35], v[34:35], s[8:9] op_sel_hi:[1,0]
	v_pk_add_f32 v[38:39], v[38:39], v[68:69]
	v_pk_add_f32 v[56:57], v[56:57], v[70:71]
	v_pk_add_f32 v[42:43], v[42:43], v[72:73]
	v_pk_add_f32 v[58:59], v[58:59], v[74:75]
	v_pk_fma_f32 v[32:33], v[62:63], s[10:11], v[32:33] op_sel_hi:[1,0,1]
	v_pk_fma_f32 v[36:37], v[60:61], s[10:11], v[36:37] op_sel_hi:[1,0,1]
	v_pk_fma_f32 v[34:35], v[66:67], s[10:11], v[34:35] op_sel_hi:[1,0,1]
	v_pk_fma_f32 v[40:41], v[64:65], s[10:11], v[40:41] op_sel_hi:[1,0,1]
	s_waitcnt lgkmcnt(1)
	v_pk_mul_f32 v[56:57], v[56:57], v[154:155]
	v_pk_mul_f32 v[38:39], v[38:39], v[152:153]
	s_waitcnt lgkmcnt(0)
; #define LAS __attribute__((address_space(3)))
; __device__ __forceinline__ float wave_sum(float v) {
;     v += __builtin_bit_cast(float, __builtin_amdgcn_update_dpp(0, __builtin_bit_cast(int, v), 0xB1, 0xf, 0xf, true));
;     v += __builtin_bit_cast(float, __builtin_amdgcn_update_dpp(0, __builtin_bit_cast(int, v), 0x4E, 0xf, 0xf, true));
;     v += __builtin_bit_cast(float, __builtin_amdgcn_update_dpp(0, __builtin_bit_cast(int, v), 0x141, 0xf, 0xf, true));
;     v += __builtin_bit_cast(float, __builtin_amdgcn_update_dpp(0, __builtin_bit_cast(int, v), 0x140, 0xf, 0xf, true));
;     const int b = __builtin_bit_cast(int, v);
; __device__ __forceinline__ void final_row(float* __restrict__ out, const RowRaw& R, const LAS float* cv  , int row, int lane) {
;     ...
;     for (int j = 0; j < 4; ++j) { const int col = c0 + 4 * j;
;         const f32x4 x1 = (t[j] - R.st.x) * R.st.y * *(const LAS f32x4*)(cv + col) + *(const LAS f32x4*)(cv + 1024 + col);
;         v[j] = x1 * ALPHA + *(const LAS f32x4*)(cv + 4096 + col) * a[j] * YINV;
;         s += (v[j].x + v[j].y) + (v[j].z + v[j].w); }
;     const float mean = wave_sum(s) * (1.f / D); float s2 = 0.f;
; #pragma unroll
;     for (int j = 0; j < 4; ++j) { v[j] = v[j] - mean; s2 += (v[j].x * v[j].x + v[j].y * v[j].y) + (v[j].z * v[j].z + v[j].w * v[j].w); }
;     const float rstd = 1.f / sqrtf(wave_sum(s2) * (1.f / D) + LN_EPS);
; #pragma unroll
;     for (int j = 0; j < 4; ++j) { const int col = c0 + 4 * j;
;         *(f32x4*)(out + (size_t)row * D + col) = v[j] * rstd * *(const LAS f32x4*)(cv + 2048 + col) + *(const LAS f32x4*)(cv + 3072 + col); }
	v_pk_mul_f32 v[58:59], v[58:59], v[158:159]
	v_pk_mul_f32 v[42:43], v[42:43], v[156:157]
	v_pk_mov_b32 v[60:61], v[32:33], v[36:37] op_sel:[1,0]
	v_mov_b32_e32 v62, v32
	v_mov_b32_e32 v63, v37
	v_pk_mov_b32 v[64:65], v[34:35], v[40:41] op_sel:[1,0]
	v_mov_b32_e32 v66, v34
	v_mov_b32_e32 v67, v41
	v_pk_fma_f32 v[68:69], v[130:131], v[102:103], v[80:81]
	v_pk_fma_f32 v[70:71], v[124:125], v[104:105], v[82:83]
	v_pk_fma_f32 v[72:73], v[136:137], v[106:107], v[84:85]
	v_pk_fma_f32 v[74:75], v[126:127], v[108:109], v[86:87]
	v_pk_mul_f32 v[56:57], v[56:57], s[8:9] op_sel_hi:[1,0]
	v_pk_mul_f32 v[38:39], v[38:39], s[8:9] op_sel_hi:[1,0]
	v_pk_mul_f32 v[58:59], v[58:59], s[8:9] op_sel_hi:[1,0]
	v_pk_mul_f32 v[42:43], v[42:43], s[8:9] op_sel_hi:[1,0]
	v_pk_add_f32 v[60:61], v[60:61], v[62:63]
	v_pk_add_f32 v[62:63], v[64:65], v[66:67]
	v_pk_fma_f32 v[56:57], v[70:71], s[10:11], v[56:57] op_sel_hi:[1,0,1]
	v_pk_fma_f32 v[38:39], v[68:69], s[10:11], v[38:39] op_sel_hi:[1,0,1]
	v_pk_fma_f32 v[58:59], v[74:75], s[10:11], v[58:59] op_sel_hi:[1,0,1]
	v_pk_fma_f32 v[42:43], v[72:73], s[10:11], v[42:43] op_sel_hi:[1,0,1]
	v_add_f32_e32 v66, v60, v61
	v_pk_add_f32 v[60:61], v[62:63], v[62:63] op_sel:[0,1] op_sel_hi:[1,0]
	v_add_f32_e32 v68, v38, v39
	v_add_f32_e32 v70, v56, v57
	v_mov_b32_e32 v73, v42
	v_mov_b32_e32 v69, v58
	v_mov_b32_e32 v71, v59
	v_add_f32_e32 v72, 0, v66
	v_mov_b32_e32 v61, v43
	v_pk_add_f32 v[64:65], v[68:69], v[70:71]
	v_pk_add_f32 v[60:61], v[72:73], v[60:61]
	s_add_i32 s4, s18, s23
	v_pk_add_f32 v[60:61], v[60:61], v[64:65]
	s_ashr_i32 s5, s4, 31
	v_add_f32_e32 v60, v60, v61
	s_lshl_b64 s[4:5], s[4:5], 12
	s_mov_b32 s23, s13
	v_add_f32_dpp v60, v60, v60 quad_perm:[1,0,3,2] row_mask:0xf bank_mask:0xf bound_ctrl:1
	s_cmp_eq_u32 s13, 32
	v_lshl_add_u64 v[202:203], v[52:53], 0, s[4:5]
	v_lshl_add_u64 v[212:213], v[210:211], 0, s[4:5]
	v_add_f32_dpp v60, v60, v60 quad_perm:[2,3,0,1] row_mask:0xf bank_mask:0xf bound_ctrl:1
	ds_read_b128 v[76:79], v184 offset:8192
	ds_read_b128 v[160:163], v184 offset:8208
	ds_read_b128 v[164:167], v184 offset:12288
	ds_read_b128 v[168:171], v184 offset:12304
	ds_read_b128 v[172:175], v184 offset:8224
	ds_read_b128 v[176:179], v184 offset:8240
	ds_read_b128 v[180:183], v184 offset:12320
	ds_read_b128 v[184:187], v184 offset:12336
	v_add_f32_dpp v60, v60, v60 row_half_mirror row_mask:0xf bank_mask:0xf bound_ctrl:1
	s_waitcnt vmcnt(0)
; #define LAS __attribute__((address_space(3)))
; __device__ __forceinline__ float wave_sum(float v) {
;     v += __builtin_bit_cast(float, __builtin_amdgcn_update_dpp(0, __builtin_bit_cast(int, v), 0xB1, 0xf, 0xf, true));
;     v += __builtin_bit_cast(float, __builtin_amdgcn_update_dpp(0, __builtin_bit_cast(int, v), 0x4E, 0xf, 0xf, true));
;     v += __builtin_bit_cast(float, __builtin_amdgcn_update_dpp(0, __builtin_bit_cast(int, v), 0x141, 0xf, 0xf, true));
;     v += __builtin_bit_cast(float, __builtin_amdgcn_update_dpp(0, __builtin_bit_cast(int, v), 0x140, 0xf, 0xf, true));
;     const int b = __builtin_bit_cast(int, v);
;     return (__builtin_bit_cast(float, __builtin_amdgcn_readlane(b, 0)) + __builtin_bit_cast(float, __builtin_amdgcn_readlane(b, 16))) + (__builtin_bit_cast(float, __builtin_amdgcn_readlane(b, 32)) + __builtin_bit_cast(float, __builtin_amdgcn_readlane(b, 48)));
; __device__ __forceinline__ void final_row(float* __restrict__ out, const RowRaw& R, const LAS float* cv  , int row, int lane) {
;     ...
;     const float mean = wave_sum(s) * (1.f / D); float s2 = 0.f;
; #pragma unroll
;     for (int j = 0; j < 4; ++j) { v[j] = v[j] - mean; s2 += (v[j].x * v[j].x + v[j].y * v[j].y) + (v[j].z * v[j].z + v[j].w * v[j].w); }
;     const float rstd = 1.f / sqrtf(wave_sum(s2) * (1.f / D) + LN_EPS);
; #pragma unroll
;     for (int j = 0; j < 4; ++j) { const int col = c0 + 4 * j;
;         *(f32x4*)(out + (size_t)row * D + col) = v[j] * rstd * *(const LAS f32x4*)(cv + 2048 + col) + *(const LAS f32x4*)(cv + 3072 + col); }
	v_mov_b64_e32 v[136:137], v[188:189]
	v_add_f32_dpp v60, v60, v60 row_mirror row_mask:0xf bank_mask:0xf bound_ctrl:1
	s_nop 0
	v_readlane_b32 s13, v60, 16
	v_readlane_b32 s14, v60, 48
	v_readlane_b32 s4, v60, 0
	v_readlane_b32 s5, v60, 32
	v_mov_b32_e32 v60, s13
	v_mov_b32_e32 v61, s14
	v_pk_add_f32 v[60:61], s[4:5], v[60:61]
	s_nop 0
	v_add_f32_e32 v60, v60, v61
	v_fmamk_f32 v33, v60, 0xba800000, v33
	v_fmac_f32_e32 v32, 0xba800000, v60
	v_fmamk_f32 v37, v60, 0xba800000, v37
	v_fmac_f32_e32 v36, 0xba800000, v60
	v_fmamk_f32 v35, v60, 0xba800000, v35
	v_fmac_f32_e32 v34, 0xba800000, v60
	v_fmamk_f32 v41, v60, 0xba800000, v41
	v_fmac_f32_e32 v40, 0xba800000, v60
	v_fmamk_f32 v39, v60, 0xba800000, v39
	v_fmac_f32_e32 v38, 0xba800000, v60
	v_fmamk_f32 v57, v60, 0xba800000, v57
	v_fmac_f32_e32 v56, 0xba800000, v60
	v_fmamk_f32 v59, v60, 0xba800000, v59
	v_fmac_f32_e32 v58, 0xba800000, v60
	v_fmamk_f32 v43, v60, 0xba800000, v43
	v_fmac_f32_e32 v42, 0xba800000, v60
	v_pk_mul_f32 v[60:61], v[36:37], v[36:37]
	v_pk_mul_f32 v[62:63], v[32:33], v[32:33]
	v_pk_mul_f32 v[64:65], v[40:41], v[40:41]
	v_pk_mul_f32 v[66:67], v[34:35], v[34:35]
	v_pk_mov_b32 v[72:73], v[62:63], v[60:61] op_sel:[1,0]
	v_mov_b32_e32 v63, v61
	v_pk_mov_b32 v[60:61], v[66:67], v[64:65] op_sel:[1,0]
	v_mov_b32_e32 v67, v65
	v_mul_f32_e32 v68, v38, v38
	v_mul_f32_e32 v70, v56, v56
	v_pk_add_f32 v[62:63], v[72:73], v[62:63]
	v_pk_add_f32 v[60:61], v[60:61], v[66:67]
	v_pk_fma_f32 v[64:65], v[38:39], v[38:39], v[68:69] op_sel_hi:[1,1,0]
	v_pk_fma_f32 v[68:69], v[56:57], v[56:57], v[70:71] op_sel_hi:[1,1,0]
	v_pk_add_f32 v[62:63], v[62:63], v[62:63] op_sel_hi:[0,1]
	v_pk_add_f32 v[60:61], v[60:61], v[60:61] op_sel_hi:[0,1]
	v_mul_f32_e32 v64, v42, v42
	v_mul_f32_e32 v68, v43, v43
	v_mul_f32_e32 v62, v58, v58
	v_mul_f32_e32 v60, v59, v59
	v_pk_add_f32 v[64:65], v[64:65], v[68:69]
	v_pk_add_f32 v[60:61], v[62:63], v[60:61]
	s_nop 0
	v_pk_add_f32 v[60:61], v[64:65], v[60:61]
	s_nop 0
	v_add_f32_e32 v60, v60, v61
	s_nop 1
	v_add_f32_dpp v60, v60, v60 quad_perm:[1,0,3,2] row_mask:0xf bank_mask:0xf bound_ctrl:1
	s_nop 1
	v_add_f32_dpp v60, v60, v60 quad_perm:[2,3,0,1] row_mask:0xf bank_mask:0xf bound_ctrl:1
	s_nop 1
	v_add_f32_dpp v60, v60, v60 row_half_mirror row_mask:0xf bank_mask:0xf bound_ctrl:1
	s_nop 1
	v_add_f32_dpp v60, v60, v60 row_mirror row_mask:0xf bank_mask:0xf bound_ctrl:1
	s_nop 0
	v_readlane_b32 s13, v60, 16
	v_readlane_b32 s14, v60, 48
	v_readlane_b32 s4, v60, 0
	v_readlane_b32 s5, v60, 32
	v_mov_b32_e32 v60, s13
	v_mov_b32_e32 v61, s14
	v_pk_add_f32 v[60:61], s[4:5], v[60:61]
	s_nop 0
	v_add_f32_e32 v60, v60, v61
	v_fmamk_f32 v60, v60, 0x3a800000, v205
	v_mul_f32_e32 v61, 0x4f800000, v60
	v_cmp_gt_f32_e32 vcc, s21, v60
	s_nop 1
	v_cndmask_b32_e32 v60, v60, v61, vcc
	v_sqrt_f32_e32 v61, v60
	s_nop 0
	v_add_u32_e32 v62, -1, v61
	v_add_u32_e32 v63, 1, v61
	v_fma_f32 v64, -v62, v61, v60
	v_fma_f32 v65, -v63, v61, v60
	v_cmp_ge_f32_e64 s[4:5], 0, v64
	s_nop 1
	v_cndmask_b32_e64 v61, v61, v62, s[4:5]
	v_cmp_lt_f32_e64 s[4:5], 0, v65
	s_nop 1
	v_cndmask_b32_e64 v61, v61, v63, s[4:5]
	v_mul_f32_e32 v62, 0x37800000, v61
	v_cndmask_b32_e32 v61, v61, v62, vcc
	v_cmp_class_f32_e32 vcc, v60, v206
	s_nop 1
	v_cndmask_b32_e32 v60, v61, v60, vcc
	v_div_scale_f32 v61, s[4:5], v60, v60, 1.0
	v_rcp_f32_e32 v63, v61
	v_div_scale_f32 v62, vcc, 1.0, v60, 1.0
	v_fma_f32 v64, -v61, v63, 1.0
	v_fmac_f32_e32 v63, v64, v63
	v_mul_f32_e32 v64, v62, v63
	v_fma_f32 v65, -v61, v64, v62
	v_fmac_f32_e32 v64, v65, v63
	v_fma_f32 v61, -v61, v64, v62
	v_div_fmas_f32 v61, v61, v63, v64
	v_div_fixup_f32 v60, v61, v60, 1.0
	v_pk_mul_f32 v[32:33], v[32:33], v[60:61] op_sel_hi:[1,0]
	v_pk_mul_f32 v[36:37], v[36:37], v[60:61] op_sel_hi:[1,0]
	v_pk_mul_f32 v[62:63], v[34:35], v[60:61] op_sel_hi:[1,0]
	v_pk_mul_f32 v[40:41], v[40:41], v[60:61] op_sel_hi:[1,0]
	v_pk_mul_f32 v[56:57], v[56:57], v[60:61] op_sel_hi:[1,0]
	v_pk_mul_f32 v[64:65], v[38:39], v[60:61] op_sel_hi:[1,0]
	v_pk_mul_f32 v[58:59], v[58:59], v[60:61] op_sel_hi:[1,0]
	v_pk_mul_f32 v[60:61], v[42:43], v[60:61] op_sel_hi:[1,0]
	s_waitcnt lgkmcnt(5)
	v_pk_fma_f32 v[34:35], v[78:79], v[36:37], v[166:167]
	v_pk_fma_f32 v[32:33], v[76:77], v[32:33], v[164:165]
	s_waitcnt lgkmcnt(4)
	v_pk_fma_f32 v[38:39], v[162:163], v[40:41], v[170:171]
	v_pk_fma_f32 v[36:37], v[160:161], v[62:63], v[168:169]
	s_waitcnt lgkmcnt(1)
	v_pk_fma_f32 v[40:41], v[172:173], v[64:65], v[180:181]
	v_pk_fma_f32 v[42:43], v[174:175], v[56:57], v[182:183]
	s_waitcnt lgkmcnt(0)
	v_pk_fma_f32 v[56:57], v[60:61], v[176:177], v[184:185]
	v_pk_fma_f32 v[58:59], v[58:59], v[178:179], v[186:187]
	ds_write_b128 v208, v[32:35]
	ds_write_b128 v208, v[36:39] offset:16
	ds_write_b128 v208, v[40:43] offset:32
	ds_write_b128 v208, v[56:59] offset:48
	ds_read_b128 v[32:35], v209
	ds_read_b128 v[36:39], v209 offset:1280
	ds_read_b128 v[40:43], v209 offset:2560
	ds_read_b128 v[56:59], v209 offset:3840
	s_waitcnt lgkmcnt(0)
	global_store_dwordx4 v[212:213], v[32:35], off
	global_store_dwordx4 v[212:213], v[36:39], off offset:1024
	global_store_dwordx4 v[212:213], v[40:43], off offset:2048
	global_store_dwordx4 v[212:213], v[56:59], off offset:3072
	v_mov_b64_e32 v[34:35], v[10:11]
	v_mov_b64_e32 v[38:39], v[6:7]
	v_mov_b64_e32 v[42:43], v[2:3]
	v_mov_b64_e32 v[32:33], v[8:9]
	v_mov_b64_e32 v[36:37], v[4:5]
	v_mov_b64_e32 v[40:41], v[0:1]
	v_mov_b64_e32 v[0:1], v[148:149]
	v_mov_b64_e32 v[4:5], v[144:145]
	v_mov_b64_e32 v[8:9], v[140:141]
	v_mov_b64_e32 v[2:3], v[150:151]
	v_mov_b64_e32 v[6:7], v[146:147]
	v_mov_b64_e32 v[10:11], v[142:143]
	s_cbranch_scc0 .LBB0_856
	s_add_i32 s44, s44, s9
	s_add_i32 s18, s18, s19
	s_cmpk_gt_i32 s44, 0xff
	s_cbranch_scc0 .LBB0_851
